# grid-barrier wait loops keep two polls in flight and leave the last one undrained
# baseline (speedup 1.0000x reference)
.Lxb_spin2_0:
	global_load_dword v242, v237, s[100:101] sc1
	s_waitcnt vmcnt(1)
	v_cmp_ge_u32_e32 vcc, v238, v236
	s_cbranch_vccnz .Lxb_done2_0
	s_sleep 1
	global_load_dword v238, v237, s[100:101] sc1
	s_waitcnt vmcnt(1)
	v_cmp_ge_u32_e32 vcc, v242, v236
	s_cbranch_vccnz .Lxb_done2_0
	s_sleep 1
	v_add_u32_e32 v239, 1, v239
	v_cmp_gt_u32_e32 vcc, 0x100000, v239
	s_cbranch_vccnz .Lxb_spin2_0

.Lxb_done2_0:
.LBB0_137:
	s_or_b64 exec, exec, s[0:1]
	s_mov_b64 s[12:13], s[46:47]
	v_mov_b32_e32 v148, v186
	s_waitcnt lgkmcnt(0)
	s_barrier
	s_load_dwordx2 s[0:1], s[12:13], 0x98

.Lxb_done2_1:
.LBB0_208:
	s_or_b64 exec, exec, s[0:1]
	v_readlane_b32 s8, v235, 0
	v_readlane_b32 s10, v235, 2
	s_mul_i32 s0, s10, 33
	s_lshr_b32 s4, s0, 6
	s_cmp_gt_i32 s10, 63
	s_cselect_b64 s[0:1], -1, 0
	s_and_b64 s[2:3], s[0:1], exec
	s_cselect_b32 s27, s4, s10
	s_ashr_i32 s17, s52, 31
	s_lshr_b32 s2, s17, 29
	s_add_i32 s2, s52, s2
	s_ashr_i32 s62, s2, 3
	s_and_b32 s2, s2, -8
	s_sub_i32 s63, s52, s2
	v_readlane_b32 s11, v235, 3
	s_mov_b32 s16, s52
	s_cmp_lt_i32 s63, 0
	v_readlane_b32 s9, v235, 1
	s_cselect_b64 s[4:5], -1, 0
	s_cmp_lt_i32 s52, s27
	s_mov_b64 s[10:11], s[46:47]
	v_writelane_b32 v235, s16, 16
	s_waitcnt lgkmcnt(0)
	s_barrier
	v_writelane_b32 v235, s17, 17
	s_cbranch_scc0 .LBB0_265
	s_cmpk_lt_i32 s16, 0x318
	v_mov_b32_e32 v8, v186
	s_cselect_b64 s[2:3], -1, 0
	s_cmpk_gt_i32 s16, 0x317
	s_nop 0
	v_readfirstlane_b32 s20, v8
	s_cbranch_scc1 .LBB0_211
	s_movk_i32 s12, 0x64
	s_and_b64 s[8:9], s[4:5], exec
	s_cselect_b32 s8, s12, 0x63
	s_mul_i32 s8, s63, s8
	s_add_i32 s8, s8, s62
	s_mul_hi_i32 s9, s8, 0x2aaaaaab
	s_lshr_b32 s12, s9, 31
	s_ashr_i32 s9, s9, 4
	s_add_i32 s9, s9, s12
	s_lshl_b32 s12, s9, 3
	s_sub_i32 s13, 0x42, s12
	s_min_u32 s13, s13, 8
	s_mulk_i32 s9, 0x60
	s_sub_i32 s14, s8, s9
	v_cvt_f32_ubyte0_e32 v1, s13
	v_cvt_f32_i32_e32 v0, s14
	v_rcp_iflag_f32_e32 v2, v1
	s_ashr_i32 s8, s14, 30
	s_or_b32 s15, s8, 1
	v_mul_f32_e32 v2, v0, v2
	v_trunc_f32_e32 v2, v2
	v_fma_f32 v0, -v2, v1, v0
	v_cvt_i32_f32_e32 v2, v2
	v_cmp_ge_f32_e64 s[8:9], |v0|, v1
	s_and_b64 s[8:9], s[8:9], exec
	s_cselect_b32 s8, s15, 0
	v_readfirstlane_b32 s9, v2
	s_add_i32 s9, s9, s8
	s_sext_i32_i8 s8, s9
	s_mul_i32 s9, s9, s13
	s_sub_i32 s9, s14, s9
	s_sext_i32_i8 s9, s9
	s_add_i32 s54, s12, s9

.Lxb_done2_2:
.LBB0_346:
	s_or_b64 exec, exec, s[0:1]
	s_mov_b64 s[0:1], s[46:47]
	v_mov_b32_e32 v66, v186
	s_waitcnt lgkmcnt(0)
	s_barrier
	s_load_dwordx2 s[2:3], s[0:1], 0x98
	v_readlane_b32 s0, v235, 16
	s_cmpk_lt_i32 s0, 0x140
	v_readlane_b32 s1, v235, 17
	s_cbranch_scc0 .LBB0_368
	s_waitcnt lgkmcnt(0)
	s_add_u32 s28, s2, 0x176f3000
	s_addc_u32 s29, s3, 0
	s_add_u32 s27, s2, 0xf1f3000
	v_and_b32_e32 v0, 63, v66
	s_addc_u32 s40, s3, 0
	s_add_u32 s30, s2, 0xd0f3000
	v_lshlrev_b32_e32 v40, 2, v0
	v_mov_b32_e32 v41, 0
	s_addc_u32 s31, s3, 0
	v_lshl_add_u64 v[0:1], s[2:3], 0, v[40:41]
	s_mov_b64 s[0:1], 0x152f3000
	s_add_u32 s34, s2, 0xc073000
	v_lshl_add_u64 v[42:43], v[0:1], 0, s[0:1]
	s_movk_i32 s41, 0x80
	v_readlane_b32 s0, v235, 16
	v_ashrrev_i32_e32 v67, 6, v66
	s_addc_u32 s35, s3, 0
	v_cmp_gt_i32_e64 s[8:9], s41, v66
	s_movk_i32 s42, 0x90
	s_mov_b32 s37, 0
	s_add_i32 s43, 0, 0x1d200
	s_mov_b32 s44, 0x1771b000
	s_add_i32 s45, 0, 0x18a00
	s_add_i32 s46, 0, 0x14200
	s_movk_i32 s47, 0x110
	s_mov_b32 s48, 0x5040100
	s_add_i32 s49, 0, 0x9800
	s_movk_i32 s50, 0x1000
	v_mov_b32_e32 v130, v41
	v_mov_b32_e32 v131, v41
	s_mov_b32 s51, s0
	v_readlane_b32 s1, v235, 17
	s_branch .LBB0_349

.Lxb_done2_3:
.LBB0_426:
	s_or_b64 exec, exec, s[0:1]
	s_mov_b64 s[0:1], s[46:47]
	s_waitcnt lgkmcnt(0)
	s_barrier
	v_mov_b32_e32 v0, v186
	s_load_dwordx2 s[0:1], s[0:1], 0x98
	v_add_u32_e32 v2, s33, v0
	s_mov_b32 s2, 0x20000
	v_cmp_gt_i32_e32 vcc, s2, v2
	s_and_saveexec_b64 s[2:3], vcc
	s_cbranch_execz .LBB0_429
	s_waitcnt lgkmcnt(0)
	s_add_u32 s8, s0, 0x152f3000
	s_addc_u32 s9, s1, 0
	s_add_u32 s10, s0, 0x176f3000
	s_addc_u32 s11, s1, 0
	v_readlane_b32 s14, v235, 16
	v_readlane_b32 s16, v235, 0
	s_add_u32 s12, s0, 0x166f3000
	v_lshlrev_b32_e32 v0, 1, v0
	v_readlane_b32 s15, v235, 17
	v_readlane_b32 s17, v235, 1
	v_readlane_b32 s18, v235, 2
	s_addc_u32 s13, s1, 0
	v_lshl_add_u32 v3, s14, 10, v0
	s_lshl_b32 s16, s18, 10
	s_mov_b64 s[14:15], 0
	v_mov_b32_e32 v1, 0
	s_mov_b32 s17, 0x1ffff
	v_readlane_b32 s19, v235, 3

.Lxb_done2_4:
.LBB0_491:
	s_or_b64 exec, exec, s[0:1]
	v_readlane_b32 s0, v235, 16
	v_readlane_b32 s1, v235, 17
	s_lshl_b32 s8, s0, 4
	v_readlane_b32 s0, v235, 0
	v_readlane_b32 s1, v235, 1
	s_mov_b64 s[14:15], s[46:47]
	s_waitcnt lgkmcnt(0)
	v_mov_b32_e32 v0, v186
	s_barrier
	s_load_dwordx2 s[0:1], s[14:15], 0x98
	s_waitcnt vmcnt(14)
	v_ashrrev_i32_e32 v68, 5, v0
	v_readlane_b32 s2, v235, 2
	v_and_b32_e32 v1, -2, v68
	s_lshl_b32 s20, s2, 4
	v_add_u32_e32 v70, s8, v1
	s_movk_i32 s2, 0x2000
	v_readlane_b32 s3, v235, 3
	v_cmp_gt_i32_e32 vcc, s2, v70
	v_writelane_b32 v235, s8, 18
	s_and_saveexec_b64 s[2:3], vcc
	s_cbranch_execz .LBB0_494
	v_bfe_u32 v69, v0, 4, 2
	v_and_b32_e32 v71, 15, v0
	v_lshlrev_b32_e32 v64, 4, v69
	v_mov_b32_e32 v65, 0
	v_lshlrev_b32_e32 v0, 8, v71
	v_mov_b32_e32 v1, v65
	s_waitcnt lgkmcnt(0)
	v_lshl_add_u64 v[66:67], s[0:1], 0, v[64:65]
	v_lshl_add_u64 v[48:49], v[66:67], 0, v[0:1]
	v_add_co_u32_e32 v18, vcc, 0x1adb000, v48
	s_mov_b64 s[8:9], 0x1adb000
	s_nop 0
	v_addc_co_u32_e32 v19, vcc, 0, v49, vcc
	v_add_co_u32_e32 v32, vcc, 0x1adc000, v48
	v_lshl_add_u64 v[16:17], v[48:49], 0, s[8:9]
	s_nop 0
	v_addc_co_u32_e32 v33, vcc, 0, v49, vcc
	v_add_co_u32_e32 v50, vcc, 0x1add000, v48
	global_load_dwordx4 v[0:3], v[16:17], off offset:64
	global_load_dwordx4 v[4:7], v[16:17], off offset:128
	global_load_dwordx4 v[8:11], v[18:19], off
	global_load_dwordx4 v[12:15], v[16:17], off offset:192
	v_addc_co_u32_e32 v51, vcc, 0, v49, vcc
	s_waitcnt vmcnt(17)
	v_add_co_u32_e32 v72, vcc, 0x1ade000, v48
	global_load_dwordx4 v[16:19], v[32:33], off
	global_load_dwordx4 v[20:23], v[32:33], off offset:64
	global_load_dwordx4 v[24:27], v[32:33], off offset:128
	global_load_dwordx4 v[28:31], v[32:33], off offset:192
	v_addc_co_u32_e32 v73, vcc, 0, v49, vcc
	global_load_dwordx4 v[32:35], v[50:51], off
	global_load_dwordx4 v[36:39], v[50:51], off offset:64
	global_load_dwordx4 v[40:43], v[50:51], off offset:128
	global_load_dwordx4 v[44:47], v[50:51], off offset:192
	s_nop 0
	global_load_dwordx4 v[48:51], v[72:73], off
	global_load_dwordx4 v[52:55], v[72:73], off offset:64
	global_load_dwordx4 v[56:59], v[72:73], off offset:128
	global_load_dwordx4 v[60:63], v[72:73], off offset:192
	s_mov_b64 s[10:11], 0x132f3000
	v_lshl_add_u64 v[66:67], v[66:67], 0, s[10:11]
	v_lshrrev_b32_e32 v64, 1, v68
	v_readlane_b32 s10, v235, 16
	v_readlane_b32 s16, v235, 0
	s_add_u32 s8, s0, 0x1971b000
	v_lshlrev_b32_e32 v68, 2, v64
	v_readlane_b32 s11, v235, 17
	v_readlane_b32 s17, v235, 1
	v_readlane_b32 s18, v235, 2
	v_lshlrev_b32_e32 v64, 5, v64
	s_addc_u32 s9, s1, 0
	v_lshlrev_b32_e32 v72, 9, v69
	v_lshl_add_u32 v73, s10, 5, v68
	s_lshl_b32 s12, s18, 5
	v_lshl_add_u32 v74, s10, 8, v64
	s_lshl_b32 s13, s18, 8
	s_mov_b64 s[10:11], 0
	s_movk_i32 s16, 0x60
	s_movk_i32 s17, 0x1fff
	v_readlane_b32 s19, v235, 3

.Lxb_done2_5:
.LBB0_553:
	s_or_b64 exec, exec, s[0:1]
	s_mov_b64 s[6:7], s[46:47]
	v_mov_b32_e32 v8, v186
	s_waitcnt lgkmcnt(0)
	s_barrier
	s_and_b64 vcc, exec, s[24:25]
	v_readfirstlane_b32 s11, v8
	s_cbranch_vccz .LBB0_573
	v_lshlrev_b32_e32 v0, 4, v8
	v_add_u32_e32 v1, 0x2000, v0
	v_ashrrev_i32_e32 v2, 31, v1
	v_lshrrev_b32_e32 v2, 22, v2
	v_add_u32_e32 v2, v1, v2
	v_ashrrev_i32_e32 v9, 10, v2
	v_mul_i32_i24_e32 v3, 0x400, v9
	v_sub_u32_e32 v1, v1, v3
	v_lshrrev_b32_e32 v3, 4, v1
	v_bitop3_b32 v1, v3, v1, 32 bitop3:0x6c
	v_ashrrev_i32_e32 v3, 31, v1
	v_lshrrev_b32_e32 v3, 26, v3
	v_add_u32_e32 v3, v1, v3
	v_ashrrev_i32_e32 v10, 6, v3
	v_and_b32_e32 v3, 0xc0, v3
	v_sub_u32_e32 v1, v1, v3
	v_mov_b32_e32 v3, 1
	v_lshlrev_b32_e32 v2, 5, v9
	v_ashrrev_i16_sdwa v1, v3, sext(v1) dst_sel:DWORD dst_unused:UNUSED_PAD src0_sel:DWORD src1_sel:BYTE_0
	v_and_b32_e32 v2, 32, v2
	v_bfe_i32 v11, v1, 0, 16
	v_add_lshl_u32 v1, v2, v11, 1
	v_lshlrev_b32_e32 v2, 3, v9
	v_and_b32_e32 v2, -16, v2
	s_load_dwordx2 s[0:1], s[6:7], 0x98
	s_load_dwordx2 s[2:3], s[6:7], 0x0
	v_add_u32_e32 v2, v10, v2
	v_and_b32_e32 v4, 3, v10
	s_mov_b32 s6, 0x1fffe0
	v_lshl_add_u32 v136, v2, 11, v1
	v_and_or_b32 v4, v2, s6, v4
	v_lshrrev_b32_e32 v5, 2, v2
	v_lshlrev_b32_e32 v2, 1, v2
	v_and_b32_e32 v5, 4, v5
	v_and_b32_e32 v2, 24, v2
	v_or3_b32 v2, v4, v5, v2
	v_lshl_add_u32 v140, v2, 11, v1
	v_bfe_i32 v2, v8, 27, 1
	v_lshrrev_b32_e32 v2, 22, v2
	v_add_u32_e32 v2, v0, v2
	v_and_b32_e32 v2, 0xfffffc00, v2
	v_sub_u32_e32 v0, v0, v2
	v_lshrrev_b32_e32 v2, 4, v0
	v_bitop3_b32 v2, v2, v0, 32 bitop3:0x6c
	v_ashrrev_i32_e32 v0, 31, v0
	v_lshrrev_b32_e32 v0, 26, v0
	v_ashrrev_i32_e32 v1, 31, v8
	v_add_u32_e32 v0, v2, v0
	v_lshrrev_b32_e32 v1, 26, v1
	v_ashrrev_i32_e32 v13, 6, v0
	v_add_u32_e32 v1, v8, v1
	v_mul_i32_i24_e32 v0, 64, v13
	v_ashrrev_i32_e32 v12, 6, v1
	v_sub_u32_e32 v0, v2, v0
	s_waitcnt lgkmcnt(0)
	s_add_u32 s33, s0, 0x1971b000
	v_lshlrev_b32_e32 v1, 5, v12
	v_ashrrev_i16_sdwa v0, v3, sext(v0) dst_sel:DWORD dst_unused:UNUSED_PAD src0_sel:DWORD src1_sel:BYTE_0
	s_addc_u32 s42, s1, 0
	v_and_b32_e32 v1, 32, v1
	v_bfe_i32 v14, v0, 0, 16
	s_add_u32 s43, s0, 0x87b000
	v_add_lshl_u32 v0, v1, v14, 1
	v_lshlrev_b32_e32 v1, 3, v12
	s_addc_u32 s44, s1, 0
	s_ashr_i32 s8, s11, 6
	v_and_b32_e32 v1, -16, v1
	s_ashr_i32 s12, s11, 8
	s_lshl_b32 s45, s8, 10
	v_add_u32_e32 v1, v13, v1
	v_and_b32_e32 v2, 3, v13
	s_lshl_b32 s7, s63, 5
	v_and_or_b32 v2, v1, s6, v2
	s_mul_i32 s6, s63, 33
	s_and_b64 s[4:5], s[4:5], exec
	s_cselect_b32 s4, s6, s7
	s_add_i32 s4, s4, s62
	s_ashr_i32 s5, s4, 31
	s_lshr_b32 s5, s5, 27
	s_add_i32 s5, s4, s5
	s_ashr_i32 s6, s5, 5
	s_and_b32 s5, s5, 0xffe0
	s_sub_i32 s4, s4, s5
	s_bfe_i32 s5, s4, 0x80000
	s_bfe_u32 s5, s5, 0x3000c
	s_add_i32 s5, s4, s5
	s_bfe_i32 s7, s5, 0x80000
	s_and_b32 s5, s5, 0xf8
	s_sub_i32 s4, s4, s5
	s_lshl_b32 s6, s6, 3
	s_sext_i32_i16 s7, s7
	s_sext_i32_i8 s4, s4
	s_lshr_b32 s10, s7, 3
	s_add_i32 s34, s6, s4
	s_ashr_i32 s35, s34, 31
	s_bfe_i64 s[6:7], s[10:11], 0x100000
	v_lshl_add_u32 v142, v1, 11, v0
	v_lshrrev_b32_e32 v3, 2, v1
	v_lshlrev_b32_e32 v1, 1, v1
	s_lshl_b64 s[4:5], s[34:35], 19
	s_lshl_b64 s[6:7], s[6:7], 19
	v_and_b32_e32 v3, 4, v3
	v_and_b32_e32 v1, 24, v1
	s_add_u32 s38, s43, s6
	v_or3_b32 v1, v2, v3, v1
	s_addc_u32 s39, s44, s7
	s_add_i32 s46, s45, 0
	v_lshl_add_u32 v146, v1, 11, v0
	s_add_i32 m0, s46, 0x10000
	v_add_u32_e32 v144, 0x40000, v142
	global_load_lds_dwordx4 v146, s[38:39]
	s_add_i32 m0, s46, 0x12000
	s_add_u32 s6, s38, 0x40000
	global_load_lds_dwordx4 v140, s[38:39]
	s_addc_u32 s7, s39, 0
	s_add_i32 m0, s46, 0x14000
	v_add_u32_e32 v138, 0x40000, v136
	global_load_lds_dwordx4 v146, s[6:7]
	s_add_i32 m0, s46, 0x16000
	s_add_u32 s36, s33, s4
	global_load_lds_dwordx4 v140, s[6:7]
	s_addc_u32 s37, s42, s5
	s_mov_b32 m0, s46
	s_add_i32 s47, s46, 0x2000
	global_load_lds_dwordx4 v142, s[36:37]
	s_mov_b32 m0, s47
	s_add_i32 s48, s46, 0x4000
	global_load_lds_dwordx4 v136, s[36:37]
	s_mov_b32 m0, s48
	s_add_i32 s49, s46, 0x6000
	global_load_lds_dwordx4 v144, s[36:37]
	s_mov_b32 m0, s49
	v_mov_b32_e32 v147, 0
	global_load_lds_dwordx4 v138, s[36:37]
	v_mov_b32_e32 v141, v147
	v_mov_b32_e32 v143, v147
	v_mov_b32_e32 v137, v147
	s_cmp_eq_u32 s12, 1
	s_mov_b32 s13, 0x40000
	s_mov_b32 s50, 0
	v_lshl_add_u64 v[6:7], s[38:39], 0, v[146:147]
	v_lshl_add_u64 v[4:5], s[38:39], 0, v[140:141]
	v_lshl_add_u64 v[0:1], s[36:37], 0, v[142:143]
	s_cselect_b64 s[4:5], -1, 0
	s_cmp_lg_u32 s12, 1
	v_lshl_add_u64 v[2:3], s[36:37], 0, v[136:137]
	s_cbranch_scc1 .LBB0_556
	s_barrier

.Lxb_done2_6:
.LBB0_626:
	s_or_b64 exec, exec, s[0:1]
	s_mov_b64 s[22:23], s[46:47]
	v_mov_b32_e32 v32, v186
	s_and_b64 vcc, exec, s[24:25]
	s_waitcnt lgkmcnt(0)
	s_barrier
	s_cbranch_vccz .LBB0_659
	s_load_dwordx2 s[24:25], s[22:23], 0x98
	s_load_dwordx2 s[26:27], s[22:23], 0x68
	v_and_b32_e32 v3, 63, v32
	v_mov_b32_e32 v35, 0
	v_lshlrev_b32_e32 v0, 3, v3
	s_waitcnt lgkmcnt(0)
	s_add_u32 s28, s24, 0x1b000
	s_addc_u32 s29, s25, 0
	s_add_u32 s0, s24, 0x9f73000
	s_addc_u32 s1, s25, 0
	v_mov_b32_e32 v1, v35
	v_lshl_add_u64 v[36:37], s[0:1], 0, v[0:1]
	v_mbcnt_hi_u32_b32 v0, -1, v187
	v_and_b32_e32 v1, 64, v0
	v_add_u32_e32 v1, 64, v1
	v_xor_b32_e32 v7, 32, v0
	v_cmp_lt_i32_e32 vcc, v7, v1
	v_ashrrev_i32_e32 v2, 6, v32
	v_and_b32_e32 v8, 1, v2
	v_cndmask_b32_e32 v7, v0, v7, vcc
	v_lshlrev_b32_e32 v104, 2, v7
	v_xor_b32_e32 v7, 16, v0
	v_cmp_lt_i32_e32 vcc, v7, v1
	v_bfe_u32 v9, v32, 4, 2
	v_lshlrev_b32_e32 v34, 2, v3
	v_cndmask_b32_e32 v7, v0, v7, vcc
	v_lshlrev_b32_e32 v105, 2, v7
	v_xor_b32_e32 v7, 8, v0
	v_cmp_lt_i32_e32 vcc, v7, v1
	v_lshlrev_b32_e32 v6, 4, v3
	v_lshlrev_b32_e32 v103, 3, v2
	v_cndmask_b32_e32 v7, v0, v7, vcc
	v_lshlrev_b32_e32 v106, 2, v7
	v_xor_b32_e32 v7, 4, v0
	v_cmp_lt_i32_e32 vcc, v7, v1
	v_cmp_eq_u32_e64 s[10:11], 0, v3
	v_mov_b32_e32 v3, v35
	v_cndmask_b32_e32 v7, v0, v7, vcc
	v_lshlrev_b32_e32 v107, 2, v7
	v_xor_b32_e32 v7, 2, v0
	v_cmp_lt_i32_e32 vcc, v7, v1
	v_and_b32_e32 v111, 15, v32
	s_movk_i32 s44, 0x2040
	v_cndmask_b32_e32 v7, v0, v7, vcc
	v_lshlrev_b32_e32 v108, 2, v7
	v_xor_b32_e32 v7, 1, v0
	v_cmp_lt_i32_e32 vcc, v7, v1
	v_mov_b32_e32 v1, v35
	v_ashrrev_i32_e32 v41, 4, v32
	v_cndmask_b32_e32 v0, v0, v7, vcc
	v_lshlrev_b32_e32 v109, 2, v0
	v_lshl_add_u32 v0, v2, 5, 0
	v_add_u32_e32 v110, 0x10240, v0
	v_lshlrev_b32_e32 v0, 10, v8
	v_lshl_add_u64 v[0:1], s[0:1], 0, v[0:1]
	v_lshlrev_b32_e32 v2, 8, v9
	v_lshl_add_u64 v[38:39], v[0:1], 0, v[2:3]
	v_lshl_or_b32 v0, v8, 2, v9
	v_ashrrev_i32_e32 v7, 7, v32
	v_mad_u32_u24 v2, v0, s44, 0
	v_lshl_add_u32 v0, v111, 2, 0
	v_lshlrev_b32_e32 v45, 2, v32
	s_add_i32 s0, 0, 0x10340
	v_add_u32_e32 v113, 0x10200, v0
	v_lshl_add_u32 v0, v7, 6, 0
	v_and_b32_e32 v4, 60, v45
	v_and_b32_e32 v5, 3, v41
	v_lshlrev_b32_e32 v112, 4, v7
	v_cmp_eq_u32_e64 s[12:13], 0, v8
	v_cmp_eq_u32_e64 s[14:15], 1, v8
	v_lshl_add_u32 v8, v7, 10, s0
	v_add_u32_e32 v7, 0x10240, v0
	v_and_b32_e32 v0, 0x7c0, v32
	v_lshl_add_u32 v0, v0, 2, 0
	v_lshlrev_b32_e32 v116, 2, v4
	v_lshlrev_b32_e32 v117, 2, v5
	v_add3_u32 v40, v0, v116, v117
	v_max_i32_e32 v0, 0x200, v32
	v_sub_u32_e32 v0, v0, v32
	v_add_u32_e32 v0, 0x1ff, v0
	s_movk_i32 s2, 0x400
	v_add_u32_e32 v98, 0, v45
	v_lshrrev_b32_e32 v1, 9, v0
	v_cmp_gt_i32_e64 s[6:7], s2, v32
	s_add_i32 s2, 0, 0x11340
	v_lshlrev_b32_e32 v114, 2, v9
	v_add_u32_e32 v118, 0x11340, v98
	v_add_u32_e32 v4, 0x12340, v98
	v_add_u32_e32 v5, 1, v1
	v_add_u32_e32 v9, -1, v1
	s_movk_i32 s0, 0x35ff
	v_lshlrev_b32_e32 v1, 11, v1
	v_add_u32_e32 v101, s2, v6
	v_cmp_lt_u32_e32 vcc, s0, v0
	v_add_u32_e32 v12, v118, v1
	v_cmp_gt_u32_e64 s[2:3], 2.0, v0
	v_add_u32_e32 v0, v4, v1
	v_cmp_lt_u32_e64 s[0:1], v12, v118
	v_cmp_lt_u32_e64 s[4:5], v0, v4
	s_or_b64 s[0:1], s[4:5], s[0:1]
	s_xor_b64 s[0:1], s[0:1], -1
	v_lshrrev_b32_e32 v11, 1, v9
	s_and_b64 s[0:1], s[0:1], s[2:3]
	v_and_b32_e32 v0, 0xfffffe, v5
	v_add_u32_e32 v11, 1, v11
	v_lshl_add_u32 v119, v0, 9, v32
	v_cmp_ne_u32_e64 s[20:21], v5, v0
	s_and_b64 s[2:3], vcc, s[0:1]
	v_lshl_add_u64 v[0:1], s[24:25], 0, v[34:35]
	s_mov_b64 s[0:1], 0xe173000
	v_readlane_b32 s36, v235, 0
	s_add_i32 s31, 0, 0x12340
	v_lshlrev_b32_e32 v3, 4, v111
	v_and_b32_e32 v10, 48, v32
	v_and_b32_e32 v4, 3, v11
	v_lshl_add_u64 v[42:43], v[0:1], 0, s[0:1]
	v_readlane_b32 s0, v235, 16
	v_readlane_b32 s38, v235, 2
	v_add_u32_e32 v99, 0x10340, v98
	v_cmp_gt_i32_e64 s[8:9], 16, v32
	v_add_u32_e32 v100, 0x10200, v98
	v_add_u32_e32 v102, s31, v6
	v_bfe_u32 v115, v41, 7, 2
	s_movk_i32 s45, 0x1ff
	v_add_u32_e32 v33, 0x200, v32
	v_cmp_lt_u32_e64 s[16:17], 5, v9
	v_and_b32_e32 v120, -4, v11
	v_cmp_ne_u32_e64 s[18:19], 0, v4
	v_lshlrev_b32_e32 v121, 12, v4
	v_lshl_add_u32 v122, s0, 6, v103
	s_lshl_b32 s5, s38, 6
	s_movk_i32 s46, 0x4000
	s_movk_i32 s47, 0x3000
	s_mov_b32 s48, 0x3fffffc
	s_mov_b32 s4, 0x3a800000
	s_mov_b32 s49, 0x800000
	s_mov_b32 s30, 0x45800000
	s_mov_b32 s50, 0xc3e00000
	v_add_u32_e32 v123, v2, v3
	v_add_u32_e32 v124, v7, v10
	s_mov_b32 s51, 0x3fb8aa3b
	s_mov_b32 s53, 0xc2ce8ed0
	s_mov_b32 s54, 0x42b17218
	s_movk_i32 s55, 0x1ff0
	v_mov_b32_e32 v44, 0x358637bd
	v_mov_b32_e32 v125, 0x43e00000
	v_add_u32_e32 v126, v8, v6
	v_mov_b32_e32 v127, 0x7f800000
	s_mov_b32 s56, s0
	v_readlane_b32 s1, v235, 17
	v_readlane_b32 s37, v235, 1
	v_readlane_b32 s39, v235, 3
	s_branch .LBB0_629

.Lxb_done2_7:
.LBB0_712:
	s_or_b64 exec, exec, s[0:1]
	v_readlane_b32 s0, v235, 0
	v_readlane_b32 s2, v235, 2
	v_readlane_b32 s3, v235, 3
	v_readlane_b32 s1, v235, 1
	s_cmp_gt_i32 s2, 63
	v_readlane_b32 s2, v235, 16
	s_cselect_b64 s[0:1], -1, 0
	s_cmp_lt_i32 s2, 32
	v_readlane_b32 s3, v235, 17
	s_cselect_b64 s[4:5], -1, 0
	s_cmp_gt_i32 s2, 31
	s_cselect_b64 s[2:3], -1, 0
	s_and_b64 s[2:3], s[2:3], s[0:1]
	s_mov_b64 s[6:7], s[46:47]
	s_mov_b64 s[0:1], -1
	s_and_b64 vcc, exec, s[2:3]
	v_readlane_b32 s46, v235, 10
	s_waitcnt lgkmcnt(0)
	s_barrier
	v_readlane_b32 s47, v235, 11
	s_cbranch_vccz .LBB0_724
	v_readlane_b32 s0, v235, 12
	v_readlane_b32 s1, v235, 13
	v_mov_b32_e32 v0, v186
	s_add_i32 s0, s52, s0
	v_readfirstlane_b32 s1, v0
	s_ashr_i32 s12, s1, 6
	s_add_i32 s0, s0, s12
	s_add_i32 s30, s0, 0x8600
	s_cmp_gt_i32 s30, 0x83ff
	s_cbranch_scc1 .LBB0_723
	s_load_dwordx4 s[0:3], s[6:7], 0x70
	s_load_dwordx2 s[8:9], s[6:7], 0x80
	s_load_dwordx2 s[10:11], s[6:7], 0x98
	s_mulk_i32 s12, 0x2100
	v_bfe_u32 v12, v0, 1, 5
	v_lshlrev_b32_e32 v1, 2, v0
	v_bfe_u32 v14, v0, 3, 3
	v_and_b32_e32 v0, 7, v0
	s_add_i32 s12, s12, 0
	v_and_b32_e32 v2, 28, v1
	v_mul_u32_u24_e32 v1, 0x220, v0
	v_lshlrev_b32_e32 v3, 2, v14
	v_lshlrev_b32_e32 v8, 4, v0
	v_add3_u32 v15, s12, v1, v3
	v_add_u32_e32 v0, s12, v8
	v_mul_u32_u24_e32 v1, 0x88, v14
	v_mov_b32_e32 v9, 0
	v_add_u32_e32 v20, v0, v1
	s_add_i32 s31, s46, 0xffffff00
	s_mov_b32 s13, 0
	v_and_b32_e32 v13, 28, v12
	v_or_b32_e32 v16, 8, v14
	v_or_b32_e32 v17, 16, v14
	v_or_b32_e32 v18, 24, v14
	v_lshlrev_b32_e32 v10, 2, v2
	v_mov_b32_e32 v11, v9
	s_mov_b32 s33, 0xc3e00000
	v_mov_b32_e32 v19, 0x43e00000
	v_add_u32_e32 v21, 0x880, v20
	v_add_u32_e32 v22, 0xcc0, v20
	s_branch .LBB0_717

.Lxb_done2_8:
.LBB0_972:
	s_or_b64 exec, exec, s[0:1]
	v_readlane_b32 s0, v235, 0
	v_readlane_b32 s2, v235, 2
	s_abs_i32 s0, s2
	s_waitcnt lgkmcnt(0)
	v_cvt_f32_u32_e32 v0, s0
	v_readlane_b32 s3, v235, 3
	s_sub_i32 s3, 0, s0
	v_readlane_b32 s1, v235, 1
	v_rcp_iflag_f32_e32 v0, v0
	s_add_i32 s1, s2, 0xaff
	s_xor_b32 s2, s1, s2
	s_abs_i32 s1, s1
	v_mul_f32_e32 v0, 0x4f7ffffe, v0
	v_cvt_u32_f32_e32 v0, v0
	s_ashr_i32 s2, s2, 31
	s_barrier
	v_readfirstlane_b32 s4, v0
	s_mul_i32 s3, s3, s4
	s_mul_hi_u32 s3, s4, s3
	s_add_i32 s4, s4, s3
	s_mul_hi_u32 s3, s1, s4
	s_mul_i32 s4, s3, s0
	s_sub_i32 s1, s1, s4
	s_add_i32 s5, s3, 1
	s_sub_i32 s4, s1, s0
	s_cmp_ge_u32 s1, s0
	s_cselect_b32 s3, s5, s3
	s_cselect_b32 s1, s4, s1
	s_add_i32 s4, s3, 1
	s_cmp_ge_u32 s1, s0
	s_cselect_b32 s0, s4, s3
	s_xor_b32 s0, s0, s2
	s_sub_i32 s2, s0, s2
	s_cmp_gt_i32 s2, 24
	s_cselect_b64 s[0:1], -1, 0
	s_cmp_lt_i32 s2, 25
	s_cbranch_scc1 .LBB0_1030
	v_readlane_b32 s4, v235, 14
	v_readlane_b32 s5, v235, 15
	v_mov_b32_e32 v0, v186
	v_readlane_b32 s10, v235, 12
	v_ashrrev_i32_e32 v2, 6, v0
	s_mov_b32 s2, 0x8000
	v_add_u32_e32 v4, s10, v2
	v_cmp_gt_i32_e32 vcc, s2, v4
	v_readlane_b32 s11, v235, 13
	s_and_saveexec_b64 s[2:3], vcc
	s_cbranch_execz .LBB0_976
	s_load_dwordx2 s[6:7], s[4:5], 0x98
	v_ashrrev_i32_e32 v3, 31, v2
	v_lshlrev_b32_e32 v0, 4, v0
	v_and_b32_e32 v6, 0x3f0, v0
	v_mov_b32_e32 v7, 0
	s_waitcnt lgkmcnt(0)
	s_add_u32 s4, s6, 0x11b000
	s_addc_u32 s5, s7, 0
	s_ashr_i32 s11, s10, 31
	v_lshl_add_u64 v[2:3], v[2:3], 0, s[10:11]
	v_lshlrev_b64 v[2:3], 10, v[2:3]
	v_or_b32_e32 v2, v2, v6
	v_lshl_add_u64 v[0:1], s[6:7], 0, v[6:7]
	s_mov_b64 s[8:9], 0xe173000
	v_lshl_add_u64 v[2:3], s[6:7], 0, v[2:3]
	s_mov_b64 s[6:7], 0xf173000
	s_ashr_i32 s47, s46, 31
	v_lshl_add_u64 v[0:1], v[0:1], 0, s[8:9]
	v_lshl_add_u64 v[2:3], v[2:3], 0, s[6:7]
	s_lshl_b64 s[6:7], s[46:47], 10
	s_mov_b64 s[8:9], 0
	s_movk_i32 s10, 0x3ff
	s_movk_i32 s11, 0x7fff

.Lxb_done2_9:
.LBB0_1029:
	s_or_b64 exec, exec, s[2:3]
	s_waitcnt lgkmcnt(0)
	s_barrier

.Lxb_done2_10:
.LBB0_1168:
	s_or_b64 exec, exec, s[0:1]
	v_readlane_b32 s0, v235, 16
	v_readlane_b32 s1, v235, 17
	s_cmpk_lt_i32 s0, 0x200
	v_readlane_b32 s0, v235, 14
	v_readlane_b32 s1, v235, 15
	v_mov_b32_e32 v8, v186
	s_waitcnt lgkmcnt(0)
	s_barrier
	s_nop 0
	v_readfirstlane_b32 s14, v8
	s_cbranch_scc0 .LBB0_1188
	v_lshlrev_b32_e32 v0, 4, v8
	v_add_u32_e32 v1, 0x2000, v0
	v_ashrrev_i32_e32 v2, 31, v1
	v_lshrrev_b32_e32 v2, 22, v2
	v_add_u32_e32 v2, v1, v2
	v_ashrrev_i32_e32 v10, 10, v2
	v_lshlrev_b32_e32 v2, 5, v10
	v_and_b32_e32 v9, 32, v2
	v_mul_i32_i24_e32 v2, 0x400, v10
	v_sub_u32_e32 v1, v1, v2
	v_lshrrev_b32_e32 v2, 4, v1
	v_bitop3_b32 v1, v2, v1, 32 bitop3:0x6c
	v_ashrrev_i32_e32 v2, 31, v1
	v_lshrrev_b32_e32 v2, 26, v2
	v_add_u32_e32 v2, v1, v2
	v_ashrrev_i32_e32 v12, 6, v2
	v_and_b32_e32 v2, 0xc0, v2
	v_lshlrev_b32_e32 v3, 3, v10
	v_sub_u32_e32 v1, v1, v2
	v_mov_b32_e32 v2, 1
	v_and_b32_e32 v3, -16, v3
	v_ashrrev_i16_sdwa v11, v2, sext(v1) dst_sel:DWORD dst_unused:UNUSED_PAD src0_sel:DWORD src1_sel:BYTE_0
	v_add_u32_e32 v3, v12, v3
	s_movk_i32 s16, 0x580
	v_add_u32_sdwa v1, v9, sext(v11) dst_sel:DWORD dst_unused:UNUSED_PAD src0_sel:DWORD src1_sel:WORD_0
	v_mul_lo_u32 v4, v3, s16
	v_add_lshl_u32 v160, v1, v4, 1
	v_ashrrev_i32_e32 v4, 31, v8
	v_lshrrev_b32_e32 v4, 26, v4
	v_add_u32_e32 v4, v8, v4
	v_ashrrev_i32_e32 v14, 6, v4
	v_lshlrev_b32_e32 v4, 5, v14
	v_and_b32_e32 v13, 32, v4
	v_bfe_i32 v4, v8, 27, 1
	v_lshrrev_b32_e32 v4, 22, v4
	v_add_u32_e32 v4, v0, v4
	v_and_b32_e32 v4, 0xfffffc00, v4
	v_sub_u32_e32 v0, v0, v4
	v_lshrrev_b32_e32 v4, 4, v0
	v_bitop3_b32 v4, v4, v0, 32 bitop3:0x6c
	v_ashrrev_i32_e32 v0, 31, v0
	v_lshrrev_b32_e32 v0, 26, v0
	v_add_u32_e32 v0, v4, v0
	v_ashrrev_i32_e32 v16, 6, v0
	v_mul_i32_i24_e32 v0, 64, v16
	v_sub_u32_e32 v0, v4, v0
	v_ashrrev_i16_sdwa v15, v2, sext(v0) dst_sel:DWORD dst_unused:UNUSED_PAD src0_sel:DWORD src1_sel:BYTE_0
	v_lshlrev_b32_e32 v2, 3, v14
	v_and_b32_e32 v2, -16, v2
	s_load_dwordx2 s[6:7], s[0:1], 0x98
	v_add_u32_e32 v2, v16, v2
	v_add_u32_sdwa v0, v13, sext(v15) dst_sel:DWORD dst_unused:UNUSED_PAD src0_sel:DWORD src1_sel:WORD_0
	v_mul_lo_u32 v4, v2, s16
	v_add_lshl_u32 v164, v0, v4, 1
	v_and_b32_e32 v4, 3, v12
	s_mov_b32 s2, 0x1ffffe0
	s_lshl_b32 s0, s47, 3
	v_and_or_b32 v4, v3, s2, v4
	v_lshrrev_b32_e32 v5, 2, v3
	v_lshlrev_b32_e32 v3, 1, v3
	s_or_b32 s59, s0, s46
	v_and_b32_e32 v5, 4, v5
	v_and_b32_e32 v3, 24, v3
	s_waitcnt lgkmcnt(0)
	s_add_u32 s23, s6, 0x11173000
	v_or3_b32 v3, v4, v5, v3
	s_addc_u32 s33, s7, 0
	v_mul_lo_u32 v3, v3, s16
	s_add_u32 s36, s6, 0x7373000
	v_add_lshl_u32 v168, v3, v1, 1
	v_and_b32_e32 v1, 3, v16
	s_addc_u32 s37, s7, 0
	s_ashr_i32 s12, s14, 6
	v_and_or_b32 v1, v2, s2, v1
	v_lshrrev_b32_e32 v3, 2, v2
	v_lshlrev_b32_e32 v2, 1, v2
	s_ashr_i32 s15, s14, 8
	s_lshl_b32 s38, s12, 10
	s_mul_i32 s0, s22, 0xb0000
	v_and_b32_e32 v3, 4, v3
	v_and_b32_e32 v2, 24, v2
	s_mul_hi_i32 s1, s22, 0xb0000
	v_or3_b32 v1, v1, v3, v2
	s_add_u32 s0, s36, s0
	v_mul_lo_u32 v1, v1, s16
	s_addc_u32 s1, s37, s1
	s_add_i32 s39, s38, 0
	v_add_lshl_u32 v170, v1, v0, 1
	v_mov_b32_e32 v188, 0x79797979
	v_mov_b32_e32 v189, 0x7c7c7c7c
	s_add_i32 m0, s39, 0x10000
	s_mul_i32 s5, s59, 0xb0000
	global_load_lds_dwordx4 v170, s[0:1]
	s_add_i32 m0, s39, 0x12000
	s_add_u32 s2, s0, 0x58000
	global_load_lds_dwordx4 v168, s[0:1]
	s_addc_u32 s3, s1, 0
	s_add_i32 m0, s39, 0x14000
	s_mul_hi_i32 s4, s59, 0xb0000
	global_load_lds_dwordx4 v170, s[2:3]
	s_add_i32 m0, s39, 0x16000
	s_add_u32 s28, s23, s5
	global_load_lds_dwordx4 v168, s[2:3]
	s_addc_u32 s29, s33, s4
	s_mov_b32 m0, s39
	s_add_i32 s40, s39, 0x2000
	global_load_lds_dwordx4 v164, s[28:29]
	s_mov_b32 m0, s40
	s_add_i32 s41, s39, 0x4000
	v_add_u32_e32 v166, 0x58000, v164
	global_load_lds_dwordx4 v160, s[28:29]
	s_mov_b32 m0, s41
	s_add_i32 s42, s39, 0x6000
	v_add_u32_e32 v162, 0x58000, v160
	global_load_lds_dwordx4 v166, s[28:29]
	s_mov_b32 m0, s42
	v_mov_b32_e32 v173, 0
	global_load_lds_dwordx4 v162, s[28:29]
	v_mov_b32_e32 v171, v173
	v_mov_b32_e32 v169, v173
	v_mov_b32_e32 v165, v173
	v_mov_b32_e32 v161, v173
	s_cmp_eq_u32 s15, 1
	s_mov_b32 s43, 0x58000
	s_mov_b32 s44, 0
	v_lshl_add_u64 v[6:7], s[0:1], 0, v[170:171]
	v_lshl_add_u64 v[2:3], s[0:1], 0, v[168:169]
	s_mov_b64 s[2:3], 0x58000
	v_lshl_add_u64 v[0:1], s[28:29], 0, v[164:165]
	s_cselect_b64 s[4:5], -1, 0
	s_cmp_lg_u32 s15, 1
	v_lshl_add_u64 v[4:5], s[28:29], 0, v[160:161]
	s_cbranch_scc1 .LBB0_1171
	s_barrier

.Lxb_done2_11:
.LBB0_1241:
	s_or_b64 exec, exec, s[0:1]
	s_waitcnt lgkmcnt(0)
	s_barrier
	v_readlane_b32 s0, v235, 18
	v_ashrrev_i32_e32 v0, 5, v186
	v_and_b32_e32 v0, -2, v0
	v_add_u32_e32 v16, s0, v0
	s_movk_i32 s0, 0x4000
	v_cmp_gt_i32_e32 vcc, s0, v16
	s_and_saveexec_b64 s[0:1], vcc
	s_cbranch_execz .LBB0_1250
	s_load_dwordx2 s[4:5], s[46:47], 0x98
	s_load_dwordx4 s[0:3], s[46:47], 0x88
	v_and_b32_e32 v0, 31, v186
	v_mov_b32_e32 v19, 0
	v_lshlrev_b32_e32 v18, 2, v0
	s_waitcnt lgkmcnt(0)
	v_lshl_add_u64 v[0:1], s[4:5], 0, v[18:19]
	s_mov_b64 s[6:7], 0x15b000
	v_lshl_add_u64 v[20:21], v[0:1], 0, s[6:7]
	v_lshlrev_b32_e32 v0, 3, v186
	v_and_b32_e32 v0, 0x1f8, v0
	v_lshlrev_b32_e32 v18, 1, v0
	v_lshl_add_u64 v[2:3], s[4:5], 0, v[18:19]
	s_mov_b64 s[6:7], 0x9f73000
	v_lshl_add_u64 v[22:23], v[2:3], 0, s[6:7]
	s_mov_b64 s[6:7], 0x1b73000
	v_mbcnt_hi_u32_b32 v1, -1, v187
	v_lshl_add_u64 v[24:25], v[2:3], 0, s[6:7]
	v_and_b32_e32 v2, 64, v1
	v_add_u32_e32 v2, 64, v2
	v_xor_b32_e32 v3, 32, v1
	v_cmp_lt_i32_e32 vcc, v3, v2
	v_lshlrev_b32_e32 v18, 2, v0
	v_lshl_add_u64 v[26:27], s[0:1], 0, v[18:19]
	v_cndmask_b32_e32 v3, v1, v3, vcc
	v_lshlrev_b32_e32 v66, 2, v3
	v_xor_b32_e32 v3, 16, v1
	v_cmp_lt_i32_e32 vcc, v3, v2
	v_lshl_add_u64 v[28:29], s[2:3], 0, v[18:19]
	s_mov_b64 s[0:1], 0
	v_cndmask_b32_e32 v3, v1, v3, vcc
	v_lshlrev_b32_e32 v67, 2, v3
	v_xor_b32_e32 v3, 8, v1
	v_cmp_lt_i32_e32 vcc, v3, v2
	v_lshlrev_b32_e32 v18, 2, v0
	s_mov_b64 s[2:3], 0x5000
	v_cndmask_b32_e32 v3, v1, v3, vcc
	v_lshlrev_b32_e32 v68, 2, v3
	v_xor_b32_e32 v3, 4, v1
	v_cmp_lt_i32_e32 vcc, v3, v2
	s_movk_i32 s6, 0x5000
	v_mov_b32_e32 v72, 0x358637bd
	v_cndmask_b32_e32 v3, v1, v3, vcc
	v_lshlrev_b32_e32 v69, 2, v3
	v_xor_b32_e32 v3, 2, v1
	v_cmp_lt_i32_e32 vcc, v3, v2
	s_mov_b32 s7, 0x800000
	s_movk_i32 s8, 0x3fff
	v_cndmask_b32_e32 v3, v1, v3, vcc
	v_lshlrev_b32_e32 v70, 2, v3
	v_xor_b32_e32 v3, 1, v1
	v_cmp_lt_i32_e32 vcc, v3, v2
	s_nop 1
	v_cndmask_b32_e32 v1, v1, v3, vcc
	v_lshlrev_b32_e32 v71, 2, v1
	s_branch .LBB0_1244
